# DSA indexer steady-state loop software-pipelined (da/db accumulators double-buffered in spare registers, tile u reduction between tile u+1 MFMAs), first operand group pre-staged so the loop waits use
# speedup vs baseline: 1.0084x; 1.0042x over previous
; __device__ __forceinline__ void dsa2_unit(LAS unsigned char* lds, const bf16* PROJ, const bf16* KIDX, const bf16* KVN, bf16* OLAT, float* sbuf, int b, int t0, int tid) {
;     ...
;         { const int ntiles = (t0 >> 5) + 1, tpw = (ntiles + 7) >> 3, tile0 = wave * tpw; int tile1 = tile0 + tpw; tile1 = tile1 < ntiles ? tile1 : ntiles;
;           const int ahead = (r & 3) + 4 * ((r >> 3) & 1), atok = ((r >> 2) & 1) + 2 * (r >> 4);
;           const bf16* qpa = PROJ + (rowb + t0 + atok) * NP + PC_QIDX + ahead * 32 + 8 * h; const bf16* qpb = qpa + (size_t)4 * NP;
;           const bf16x8 A0a = *(const bf16x8*)qpa, A1a = *(const bf16x8*)(qpa + 16), A0b = *(const bf16x8*)qpb, A1b = *(const bf16x8*)(qpb + 16);
;           float wq[32];
; #pragma unroll
;           for (int gq = 0; gq < 4; ++gq) { const v4u w0 = *(const v4u*)(PROJ + (rowb + t0 + h + 2 * gq) * NP + PC_WIDX);
;               wq[8 * gq] = 0.5f * bflo(w0.x); wq[8 * gq + 1] = 0.5f * bfhi(w0.x); wq[8 * gq + 2] = 0.5f * bflo(w0.y); wq[8 * gq + 3] = 0.5f * bfhi(w0.y); wq[8 * gq + 4] = 0.5f * bflo(w0.z); wq[8 * gq + 5] = 0.5f * bfhi(w0.z); wq[8 * gq + 6] = 0.5f * bflo(w0.w); wq[8 * gq + 7] = 0.5f * bfhi(w0.w); }
;           v4u A0c = {0u, 0u, 0u, 0u}, A1c = {0u, 0u, 0u, 0u};
;           if (r < 8) { const bf16* qrow = PROJ + (rowb + t0 + (r >> 2) + 2 * (r & 3)) * NP; const v4u wv = *(const v4u*)(qrow + PC_WIDX);
;               const float wl_[8] = {bflo(wv.x), bfhi(wv.x), bflo(wv.y), bfhi(wv.y), bflo(wv.z), bfhi(wv.z), bflo(wv.w), bfhi(wv.w)};
;               float a0[8], a1[8];
; #pragma unroll
;               for (int j = 0; j < 8; ++j) { a0[j] = 0.f; a1[j] = 0.f; }
; #pragma unroll
;               for (int hd = 0; hd < 8; ++hd) { const v4u q0 = *(const v4u*)(qrow + PC_QIDX + hd * 32 + 8 * h), q1 = *(const v4u*)(qrow + PC_QIDX + hd * 32 + 16 + 8 * h); const float hw = 0.5f * wl_[hd];
;                   a0[0] += hw * bflo(q0.x); a0[1] += hw * bfhi(q0.x); a0[2] += hw * bflo(q0.y); a0[3] += hw * bfhi(q0.y); a0[4] += hw * bflo(q0.z); a0[5] += hw * bfhi(q0.z); a0[6] += hw * bflo(q0.w); a0[7] += hw * bfhi(q0.w);
;                   a1[0] += hw * bflo(q1.x); a1[1] += hw * bfhi(q1.x); a1[2] += hw * bflo(q1.y); a1[3] += hw * bfhi(q1.y); a1[4] += hw * bflo(q1.z); a1[5] += hw * bfhi(q1.z); a1[6] += hw * bflo(q1.w); a1[7] += hw * bfhi(q1.w); }
.LBB0_706:
	s_or_b64 exec, exec, s[2:3]
	s_lshr_b32 s1, s1, 3
	s_add_i32 s2, s1, 8
	s_lshr_b32 s4, s2, 3
	s_mul_i32 s2, s0, s4
	s_add_i32 s3, s2, s4
	s_add_i32 s1, s1, 1
	v_mov_b32_e32 v139, v128
	s_min_i32 s1, s3, s1
	v_lshlrev_b64 v[16:17], 18, v[138:139]
	s_cmp_ge_i32 s2, s1
	v_lshl_add_u64 v[140:141], s[80:81], 0, v[16:17]
	s_mov_b32 s12, 0x20000
	s_mov_b32 s13, 0x30000
	s_cbranch_scc1 .LBB0_720
	s_ashr_i32 s3, s2, 31
	s_lshl_b64 s[6:7], s[2:3], 5
	s_add_u32 s3, s6, s22
	s_addc_u32 s5, s7, 0
	v_or_b32_e32 v16, s3, v28
	v_mov_b32_e32 v17, s5
	v_lshlrev_b64 v[16:17], 6, v[16:17]
	v_lshl_add_u64 v[16:17], s[78:79], 0, v[16:17]
	v_mov_b32_e32 v25, v128
	v_lshl_add_u64 v[142:143], v[16:17], 0, v[24:25]
	s_waitcnt vmcnt(0)
	v_lshlrev_b32_e32 v16, 16, v12
	v_and_b32_e32 v12, 0xffff0000, v12
	v_mul_f32_e32 v157, 0.5, v12
	v_lshlrev_b32_e32 v12, 16, v13
	v_mul_f32_e32 v155, 0.5, v12
	v_and_b32_e32 v12, 0xffff0000, v13
	v_mul_f32_e32 v154, 0.5, v12
	v_lshlrev_b32_e32 v12, 16, v14
	v_mul_f32_e32 v153, 0.5, v12
	v_and_b32_e32 v12, 0xffff0000, v14
	v_mul_f32_e32 v152, 0.5, v12
	v_lshlrev_b32_e32 v12, 16, v15
	v_mul_f32_e32 v151, 0.5, v12
	v_and_b32_e32 v12, 0xffff0000, v15
	v_mul_f32_e32 v139, 0.5, v12
	v_lshlrev_b32_e32 v12, 16, v8
	v_and_b32_e32 v8, 0xffff0000, v8
	v_mul_f32_e32 v165, 0.5, v8
	v_lshlrev_b32_e32 v8, 16, v9
	v_mul_f32_e32 v164, 0.5, v8
	v_and_b32_e32 v8, 0xffff0000, v9
	v_mul_f32_e32 v163, 0.5, v8
	v_lshlrev_b32_e32 v8, 16, v10
	v_mul_f32_e32 v162, 0.5, v8
	v_and_b32_e32 v8, 0xffff0000, v10
	v_mul_f32_e32 v161, 0.5, v8
	v_lshlrev_b32_e32 v8, 16, v11
	v_mul_f32_e32 v160, 0.5, v8
	v_and_b32_e32 v8, 0xffff0000, v11
	v_mul_f32_e32 v159, 0.5, v8
	v_lshlrev_b32_e32 v8, 16, v4
	v_and_b32_e32 v4, 0xffff0000, v4
	v_mul_f32_e32 v173, 0.5, v4
	v_lshlrev_b32_e32 v4, 16, v5
	v_mul_f32_e32 v172, 0.5, v4
	v_and_b32_e32 v4, 0xffff0000, v5
	v_mul_f32_e32 v171, 0.5, v4
	v_lshlrev_b32_e32 v4, 16, v6
	v_mul_f32_e32 v170, 0.5, v4
	v_and_b32_e32 v4, 0xffff0000, v6
	v_mul_f32_e32 v169, 0.5, v4
	v_lshlrev_b32_e32 v4, 16, v7
	v_mul_f32_e32 v168, 0.5, v4
	v_and_b32_e32 v4, 0xffff0000, v7
	v_mul_f32_e32 v167, 0.5, v4
	v_lshlrev_b32_e32 v4, 16, v0
	v_and_b32_e32 v0, 0xffff0000, v0
	v_mul_f32_e32 v181, 0.5, v0
	v_lshlrev_b32_e32 v0, 16, v1
	v_mul_f32_e32 v180, 0.5, v0
	v_and_b32_e32 v0, 0xffff0000, v1
	s_add_i32 s3, s1, -1
	s_add_i32 s5, s2, 1
	v_mul_f32_e32 v179, 0.5, v0
	v_lshlrev_b32_e32 v0, 16, v2
	s_min_i32 s5, s5, s3
	v_mul_f32_e32 v178, 0.5, v0
	v_and_b32_e32 v0, 0xffff0000, v2
	s_sub_i32 s6, s5, s2
	v_mul_f32_e32 v177, 0.5, v0
	v_lshlrev_b32_e32 v0, 16, v3
	s_ashr_i32 s7, s6, 31
	s_add_i32 s5, s2, 2
	v_mul_f32_e32 v176, 0.5, v0
	v_and_b32_e32 v0, 0xffff0000, v3
	s_lshl_b64 s[6:7], s[6:7], 11
	s_min_i32 s5, s5, s3
	v_mul_f32_e32 v175, 0.5, v0
	v_lshl_add_u64 v[0:1], v[142:143], 0, s[6:7]
	s_sub_i32 s6, s5, s2
	s_ashr_i32 s7, s6, 31
	s_add_i32 s5, s2, 3
	s_lshl_b64 s[6:7], s[6:7], 11
	s_min_i32 s5, s5, s3
	v_mov_b64_e32 v[100:101], v[188:189]
	v_mov_b64_e32 v[102:103], v[190:191]
	v_mov_b64_e32 v[96:97], v[192:193]
	v_mov_b64_e32 v[98:99], v[194:195]
	v_mov_b64_e32 v[92:93], v[196:197]
	v_mov_b64_e32 v[94:95], v[198:199]
	v_mov_b64_e32 v[88:89], v[200:201]
	v_mov_b64_e32 v[90:91], v[202:203]
	v_lshl_add_u64 v[0:1], v[142:143], 0, s[6:7]
	s_sub_i32 s6, s5, s2
	s_ashr_i32 s7, s6, 31
	s_lshl_b64 s[6:7], s[6:7], 11
	v_mov_b64_e32 v[84:85], v[204:205]
	v_mov_b64_e32 v[86:87], v[206:207]
	v_mov_b64_e32 v[80:81], v[208:209]
	v_mov_b64_e32 v[82:83], v[210:211]
	v_lshl_add_u64 v[0:1], v[142:143], 0, s[6:7]
	v_mov_b64_e32 v[76:77], v[220:221]
	v_mov_b64_e32 v[78:79], v[222:223]
	v_mov_b64_e32 v[72:73], v[224:225]
	v_mov_b64_e32 v[74:75], v[226:227]
	s_add_i32 s5, s2, 8
	v_mul_f32_e32 v158, 0.5, v16
	v_mul_f32_e32 v166, 0.5, v12
	v_mul_f32_e32 v174, 0.5, v8
	v_mul_f32_e32 v182, 0.5, v4
	s_cmp_gt_i32 s5, s1
	v_lshlrev_b32_e32 v146, 15, v29
	v_lshlrev_b32_e32 v144, 2, v28
	s_cbranch_scc1 .LBB0_711
	v_mov_b32_e32 v145, v128
	s_mul_i32 s5, s0, s4
	v_lshl_add_u64 v[0:1], v[140:141], 0, v[144:145]
	v_mov_b32_e32 v147, v128
	s_lshl_b32 s5, s5, 5
	v_lshl_add_u64 v[148:149], v[0:1], 0, v[146:147]
	s_mov_b64 s[84:85], 0x10000
	s_mov_b64 s[86:87], 0x20000
	s_mov_b64 s[88:89], 0x30000
	s_mov_b32 s4, 5
	s_add_i32 s6, s5, 0xe0
; #define IDX_LOADG(BG, tb) do { _Pragma("unroll") for (int u = 0; u < 4; ++u) { int tt_ = (tb) + u; tt_ = tt_ < tile1 ? tt_ : tile1 - 1;        \
;               const bf16* kn = kp + (size_t)(tt_ - tile0) * 1024; BG[u][0] = *(const bf16x8*)kn; BG[u][1] = *(const bf16x8*)(kn + 16); } } while (0)
; #define IDX_TILES_NG(BG, tb) do { _Pragma("unroll") for (int u = 0; u < 4; ++u) IDX_ONE(BG, u, (tb) + u) } while (0)
; __device__ __forceinline__ void dsa2_unit(LAS unsigned char* lds, const bf16* PROJ, const bf16* KIDX, const bf16* KVN, bf16* OLAT, float* sbuf, int b, int t0, int tid) {
;     ...
;           if (tile0 < tile1) { bf16x8 BA[4][2], BB[4][2];
;               IDX_LOADG(BA, tile0);
;               int tileb = tile0;
;               for (; tileb + 8 <= tile1; tileb += 8) {
;                   IDX_LOADG(BB, tileb + 4);
;                   IDX_TILES_NG(BA, tileb);
;                   IDX_LOADG(BA, tileb + 8);
;                   IDX_TILES_NG(BB, tileb + 4); }
.LBB0_709:
	s_add_i32 s10, s4, -1
	s_ashr_i32 s11, s10, 31
	s_lshl_b64 s[10:11], s[10:11], 11
	v_lshl_add_u64 v[208:209], v[142:143], 0, s[10:11]
	global_load_dwordx4 v[134:137], v[208:209], off
	global_load_dwordx4 v[130:133], v[208:209], off offset:32
	s_ashr_i32 s5, s4, 31
	s_lshl_b64 s[10:11], s[4:5], 11
	v_lshl_add_u64 v[208:209], v[142:143], 0, s[10:11]
	global_load_dwordx4 v[124:127], v[208:209], off
	global_load_dwordx4 v[120:123], v[208:209], off offset:32
	s_add_i32 s10, s4, 1
	s_ashr_i32 s11, s10, 31
	s_lshl_b64 s[10:11], s[10:11], 11
	v_lshl_add_u64 v[208:209], v[142:143], 0, s[10:11]
	global_load_dwordx4 v[116:119], v[208:209], off
	global_load_dwordx4 v[112:115], v[208:209], off offset:32
	s_add_i32 s10, s4, 2
	s_ashr_i32 s11, s10, 31
	s_lshl_b64 s[10:11], s[10:11], 11
	v_lshl_add_u64 v[208:209], v[142:143], 0, s[10:11]
	global_load_dwordx4 v[108:111], v[208:209], off
	global_load_dwordx4 v[104:107], v[208:209], off offset:32
	s_add_i32 s10, s6, 0xffffff20
	s_ashr_i32 s11, s10, 31
	v_lshl_add_u64 v[200:201], s[10:11], 2, v[148:149]
	v_lshl_add_u64 v[202:203], v[200:201], 0, s[84:85]
	v_lshl_add_u64 v[204:205], v[200:201], 0, s[86:87]
	v_lshl_add_u64 v[206:207], v[200:201], 0, s[88:89]
	s_add_i32 s7, s2, s4
	s_waitcnt vmcnt(35)
	v_mfma_f32_32x32x16_bf16 v[16:31], v[56:59], v[100:103], 0
	v_mfma_f32_32x32x16_bf16 v[0:15], v[60:63], v[100:103], 0
	v_mfma_f32_32x32x16_bf16 v[32:47], v[64:67], v[100:103], 0
	s_waitcnt vmcnt(34)
	v_mfma_f32_32x32x16_bf16 v[16:31], v[48:51], v[96:99], v[16:31]
	v_mfma_f32_32x32x16_bf16 v[0:15], v[52:55], v[96:99], v[0:15]
	v_mfma_f32_32x32x16_bf16 v[32:47], v[68:71], v[96:99], v[32:47]
	s_waitcnt vmcnt(33)
	v_mfma_f32_32x32x16_bf16 v[184:199], v[56:59], v[92:95], 0
	v_mfma_f32_32x32x16_bf16 v[220:235], v[60:63], v[92:95], 0
	s_nop 9
	v_fma_f32 v16, v158, |v16|, v32
	v_fma_f32 v24, v166, |v24|, v33
	v_fma_f32 v0, v174, |v0|, v34
	v_fma_f32 v8, v182, |v8|, v35
	v_mfma_f32_32x32x16_bf16 v[32:47], v[64:67], v[92:95], 0
	v_fma_f32 v16, v157, |v17|, v16
	v_fma_f32 v24, v165, |v25|, v24
	v_fma_f32 v0, v173, |v1|, v0
	v_fma_f32 v8, v181, |v9|, v8
	v_fma_f32 v16, v155, |v18|, v16
	v_fma_f32 v24, v164, |v26|, v24
	v_fma_f32 v0, v172, |v2|, v0
	v_fma_f32 v8, v180, |v10|, v8
	s_waitcnt vmcnt(32)
	v_mfma_f32_32x32x16_bf16 v[184:199], v[48:51], v[88:91], v[184:199]
	v_fma_f32 v16, v154, |v19|, v16
	v_fma_f32 v24, v163, |v27|, v24
	v_fma_f32 v0, v171, |v3|, v0
	v_fma_f32 v8, v179, |v11|, v8
	v_fma_f32 v16, v153, |v20|, v16
	v_fma_f32 v24, v162, |v28|, v24
	v_fma_f32 v0, v170, |v4|, v0
	v_fma_f32 v8, v178, |v12|, v8
	v_fma_f32 v16, v152, |v21|, v16
	v_mfma_f32_32x32x16_bf16 v[220:235], v[52:55], v[88:91], v[220:235]
	v_fma_f32 v24, v161, |v29|, v24
	v_fma_f32 v0, v169, |v5|, v0
	v_fma_f32 v8, v177, |v13|, v8
	v_fma_f32 v16, v151, |v22|, v16
	v_fma_f32 v24, v160, |v30|, v24
	v_fma_f32 v0, v168, |v6|, v0
	v_fma_f32 v8, v176, |v14|, v8
	v_fma_f32 v16, v139, |v23|, v16
	v_fma_f32 v24, v159, |v31|, v24
	v_mfma_f32_32x32x16_bf16 v[32:47], v[68:71], v[88:91], v[32:47]
	v_fma_f32 v0, v167, |v7|, v0
	v_fma_f32 v8, v175, |v15|, v8
	v_ashrrev_i32_e32 v210, 31, v16
	v_bitop3_b32 v16, v210, v16, s47 bitop3:0x36
	global_store_dword v[200:201], v16, off
	v_ashrrev_i32_e32 v211, 31, v24
	v_bitop3_b32 v24, v211, v24, s47 bitop3:0x36
	global_store_dword v[202:203], v24, off
	v_ashrrev_i32_e32 v210, 31, v0
	v_bitop3_b32 v0, v210, v0, s47 bitop3:0x36
	global_store_dword v[204:205], v0, off
	v_ashrrev_i32_e32 v211, 31, v8
	v_bitop3_b32 v8, v211, v8, s47 bitop3:0x36
	global_store_dword v[206:207], v8, off
	s_waitcnt vmcnt(35)
	v_mfma_f32_32x32x16_bf16 v[16:31], v[56:59], v[84:87], 0
	v_mfma_f32_32x32x16_bf16 v[0:15], v[60:63], v[84:87], 0
	s_nop 9
	v_fma_f32 v184, v158, |v184|, v32
	v_fma_f32 v192, v166, |v192|, v33
	v_fma_f32 v220, v174, |v220|, v34
	v_fma_f32 v228, v182, |v228|, v35
	v_mfma_f32_32x32x16_bf16 v[32:47], v[64:67], v[84:87], 0
	v_fma_f32 v184, v157, |v185|, v184
	v_fma_f32 v192, v165, |v193|, v192
	v_fma_f32 v220, v173, |v221|, v220
	v_fma_f32 v228, v181, |v229|, v228
	v_fma_f32 v184, v155, |v186|, v184
	v_fma_f32 v192, v164, |v194|, v192
	v_fma_f32 v220, v172, |v222|, v220
	v_fma_f32 v228, v180, |v230|, v228
	s_waitcnt vmcnt(34)
	v_mfma_f32_32x32x16_bf16 v[16:31], v[48:51], v[80:83], v[16:31]
	v_fma_f32 v184, v154, |v187|, v184
	v_fma_f32 v192, v163, |v195|, v192
	v_fma_f32 v220, v171, |v223|, v220
	v_fma_f32 v228, v179, |v231|, v228
	v_fma_f32 v184, v153, |v188|, v184
	v_fma_f32 v192, v162, |v196|, v192
	v_fma_f32 v220, v170, |v224|, v220
	v_fma_f32 v228, v178, |v232|, v228
	v_fma_f32 v184, v152, |v189|, v184
	v_mfma_f32_32x32x16_bf16 v[0:15], v[52:55], v[80:83], v[0:15]
	v_fma_f32 v192, v161, |v197|, v192
	v_fma_f32 v220, v169, |v225|, v220
	v_fma_f32 v228, v177, |v233|, v228
	v_fma_f32 v184, v151, |v190|, v184
	v_fma_f32 v192, v160, |v198|, v192
	v_fma_f32 v220, v168, |v226|, v220
	v_fma_f32 v228, v176, |v234|, v228
	v_fma_f32 v184, v139, |v191|, v184
	v_fma_f32 v192, v159, |v199|, v192
	v_mfma_f32_32x32x16_bf16 v[32:47], v[68:71], v[80:83], v[32:47]
	v_fma_f32 v220, v167, |v227|, v220
	v_fma_f32 v228, v175, |v235|, v228
	v_ashrrev_i32_e32 v210, 31, v184
	v_bitop3_b32 v184, v210, v184, s47 bitop3:0x36
	global_store_dword v[200:201], v184, off offset:128
	v_ashrrev_i32_e32 v211, 31, v192
	v_bitop3_b32 v192, v211, v192, s47 bitop3:0x36
	global_store_dword v[202:203], v192, off offset:128
	v_ashrrev_i32_e32 v210, 31, v220
	v_bitop3_b32 v220, v210, v220, s47 bitop3:0x36
	global_store_dword v[204:205], v220, off offset:128
	v_ashrrev_i32_e32 v211, 31, v228
	v_bitop3_b32 v228, v211, v228, s47 bitop3:0x36
	global_store_dword v[206:207], v228, off offset:128
	s_waitcnt vmcnt(37)
; #define IDX_LOADG(BG, tb) do { _Pragma("unroll") for (int u = 0; u < 4; ++u) { int tt_ = (tb) + u; tt_ = tt_ < tile1 ? tt_ : tile1 - 1;        \
;               const bf16* kn = kp + (size_t)(tt_ - tile0) * 1024; BG[u][0] = *(const bf16x8*)kn; BG[u][1] = *(const bf16x8*)(kn + 16); } } while (0)
; #define IDX_TILES_NG(BG, tb) do { _Pragma("unroll") for (int u = 0; u < 4; ++u) IDX_ONE(BG, u, (tb) + u) } while (0)
; __device__ __forceinline__ void dsa2_unit(LAS unsigned char* lds, const bf16* PROJ, const bf16* KIDX, const bf16* KVN, bf16* OLAT, float* sbuf, int b, int t0, int tid) {
;     ...
;           if (tile0 < tile1) { bf16x8 BA[4][2], BB[4][2];
;               IDX_LOADG(BA, tile0);
;               int tileb = tile0;
;               for (; tileb + 8 <= tile1; tileb += 8) {
;                   IDX_LOADG(BB, tileb + 4);
;                   IDX_TILES_NG(BA, tileb);
;                   IDX_LOADG(BA, tileb + 8);
;                   IDX_TILES_NG(BB, tileb + 4); }
	v_mfma_f32_32x32x16_bf16 v[184:199], v[56:59], v[76:79], 0
	v_mfma_f32_32x32x16_bf16 v[220:235], v[60:63], v[76:79], 0
	s_nop 9
	v_fma_f32 v16, v158, |v16|, v32
	v_fma_f32 v24, v166, |v24|, v33
	v_fma_f32 v0, v174, |v0|, v34
	v_fma_f32 v8, v182, |v8|, v35
	v_mfma_f32_32x32x16_bf16 v[32:47], v[64:67], v[76:79], 0
	v_fma_f32 v16, v157, |v17|, v16
	v_fma_f32 v24, v165, |v25|, v24
	v_fma_f32 v0, v173, |v1|, v0
	v_fma_f32 v8, v181, |v9|, v8
	v_fma_f32 v16, v155, |v18|, v16
	v_fma_f32 v24, v164, |v26|, v24
	v_fma_f32 v0, v172, |v2|, v0
	v_fma_f32 v8, v180, |v10|, v8
	s_waitcnt vmcnt(36)
	v_mfma_f32_32x32x16_bf16 v[184:199], v[48:51], v[72:75], v[184:199]
	v_fma_f32 v16, v154, |v19|, v16
	v_fma_f32 v24, v163, |v27|, v24
	v_fma_f32 v0, v171, |v3|, v0
	v_fma_f32 v8, v179, |v11|, v8
	v_fma_f32 v16, v153, |v20|, v16
	v_fma_f32 v24, v162, |v28|, v24
	v_fma_f32 v0, v170, |v4|, v0
	v_fma_f32 v8, v178, |v12|, v8
	v_fma_f32 v16, v152, |v21|, v16
	v_mfma_f32_32x32x16_bf16 v[220:235], v[52:55], v[72:75], v[220:235]
	v_fma_f32 v24, v161, |v29|, v24
	v_fma_f32 v0, v169, |v5|, v0
	v_fma_f32 v8, v177, |v13|, v8
	v_fma_f32 v16, v151, |v22|, v16
	v_fma_f32 v24, v160, |v30|, v24
	v_fma_f32 v0, v168, |v6|, v0
	v_fma_f32 v8, v176, |v14|, v8
	v_fma_f32 v16, v139, |v23|, v16
	v_fma_f32 v24, v159, |v31|, v24
	v_mfma_f32_32x32x16_bf16 v[32:47], v[68:71], v[72:75], v[32:47]
	v_fma_f32 v0, v167, |v7|, v0
	v_fma_f32 v8, v175, |v15|, v8
	v_ashrrev_i32_e32 v210, 31, v16
	v_bitop3_b32 v16, v210, v16, s47 bitop3:0x36
	global_store_dword v[200:201], v16, off offset:256
	v_ashrrev_i32_e32 v211, 31, v24
	v_bitop3_b32 v24, v211, v24, s47 bitop3:0x36
	global_store_dword v[202:203], v24, off offset:256
	v_ashrrev_i32_e32 v210, 31, v0
	v_bitop3_b32 v0, v210, v0, s47 bitop3:0x36
	global_store_dword v[204:205], v0, off offset:256
	v_ashrrev_i32_e32 v211, 31, v8
	v_bitop3_b32 v8, v211, v8, s47 bitop3:0x36
	global_store_dword v[206:207], v8, off offset:256
	s_add_i32 s8, s7, 3
	s_min_i32 s8, s8, s3
	s_sub_i32 s8, s8, s2
	s_ashr_i32 s9, s8, 31
	s_lshl_b64 s[8:9], s[8:9], 11
	v_lshl_add_u64 v[208:209], v[142:143], 0, s[8:9]
	global_load_dwordx4 v[100:103], v[208:209], off
	global_load_dwordx4 v[96:99], v[208:209], off offset:32
	s_add_i32 s8, s7, 4
	s_min_i32 s8, s8, s3
	s_sub_i32 s8, s8, s2
	s_ashr_i32 s9, s8, 31
	s_lshl_b64 s[8:9], s[8:9], 11
	v_lshl_add_u64 v[208:209], v[142:143], 0, s[8:9]
	global_load_dwordx4 v[92:95], v[208:209], off
	global_load_dwordx4 v[88:91], v[208:209], off offset:32
	s_add_i32 s8, s7, 5
	s_min_i32 s8, s8, s3
	s_sub_i32 s8, s8, s2
	s_ashr_i32 s9, s8, 31
	s_lshl_b64 s[8:9], s[8:9], 11
	v_lshl_add_u64 v[208:209], v[142:143], 0, s[8:9]
	global_load_dwordx4 v[84:87], v[208:209], off
	global_load_dwordx4 v[80:83], v[208:209], off offset:32
	s_add_i32 s8, s7, 6
	s_min_i32 s8, s8, s3
	s_sub_i32 s8, s8, s2
	s_ashr_i32 s9, s8, 31
	s_lshl_b64 s[8:9], s[8:9], 11
	v_lshl_add_u64 v[208:209], v[142:143], 0, s[8:9]
	global_load_dwordx4 v[76:79], v[208:209], off
	global_load_dwordx4 v[72:75], v[208:209], off offset:32
	s_waitcnt vmcnt(27)
	v_mfma_f32_32x32x16_bf16 v[16:31], v[56:59], v[134:137], 0
	v_mfma_f32_32x32x16_bf16 v[0:15], v[60:63], v[134:137], 0
	s_nop 9
	v_fma_f32 v184, v158, |v184|, v32
	v_fma_f32 v192, v166, |v192|, v33
	v_fma_f32 v220, v174, |v220|, v34
	v_fma_f32 v228, v182, |v228|, v35
	v_mfma_f32_32x32x16_bf16 v[32:47], v[64:67], v[134:137], 0
	v_fma_f32 v184, v157, |v185|, v184
	v_fma_f32 v192, v165, |v193|, v192
	v_fma_f32 v220, v173, |v221|, v220
	v_fma_f32 v228, v181, |v229|, v228
	v_fma_f32 v184, v155, |v186|, v184
	v_fma_f32 v192, v164, |v194|, v192
	v_fma_f32 v220, v172, |v222|, v220
	v_fma_f32 v228, v180, |v230|, v228
	s_waitcnt vmcnt(26)
	v_mfma_f32_32x32x16_bf16 v[16:31], v[48:51], v[130:133], v[16:31]
	v_fma_f32 v184, v154, |v187|, v184
	v_fma_f32 v192, v163, |v195|, v192
	v_fma_f32 v220, v171, |v223|, v220
	v_fma_f32 v228, v179, |v231|, v228
	v_fma_f32 v184, v153, |v188|, v184
	v_fma_f32 v192, v162, |v196|, v192
	v_fma_f32 v220, v170, |v224|, v220
	v_fma_f32 v228, v178, |v232|, v228
	v_fma_f32 v184, v152, |v189|, v184
	v_mfma_f32_32x32x16_bf16 v[0:15], v[52:55], v[130:133], v[0:15]
	v_fma_f32 v192, v161, |v197|, v192
	v_fma_f32 v220, v169, |v225|, v220
	v_fma_f32 v228, v177, |v233|, v228
	v_fma_f32 v184, v151, |v190|, v184
	v_fma_f32 v192, v160, |v198|, v192
	v_fma_f32 v220, v168, |v226|, v220
	v_fma_f32 v228, v176, |v234|, v228
	v_fma_f32 v184, v139, |v191|, v184
	v_fma_f32 v192, v159, |v199|, v192
	v_mfma_f32_32x32x16_bf16 v[32:47], v[68:71], v[130:133], v[32:47]
	v_fma_f32 v220, v167, |v227|, v220
	v_fma_f32 v228, v175, |v235|, v228
	v_ashrrev_i32_e32 v210, 31, v184
	v_bitop3_b32 v184, v210, v184, s47 bitop3:0x36
	global_store_dword v[200:201], v184, off offset:384
	v_ashrrev_i32_e32 v211, 31, v192
	v_bitop3_b32 v192, v211, v192, s47 bitop3:0x36
	global_store_dword v[202:203], v192, off offset:384
	v_ashrrev_i32_e32 v210, 31, v220
	v_bitop3_b32 v220, v210, v220, s47 bitop3:0x36
	global_store_dword v[204:205], v220, off offset:384
	v_ashrrev_i32_e32 v211, 31, v228
	v_bitop3_b32 v228, v211, v228, s47 bitop3:0x36
	global_store_dword v[206:207], v228, off offset:384
	s_waitcnt vmcnt(29)
	v_mfma_f32_32x32x16_bf16 v[184:199], v[56:59], v[124:127], 0
	v_mfma_f32_32x32x16_bf16 v[220:235], v[60:63], v[124:127], 0
	s_nop 9
	v_fma_f32 v16, v158, |v16|, v32
	v_fma_f32 v24, v166, |v24|, v33
	v_fma_f32 v0, v174, |v0|, v34
	v_fma_f32 v8, v182, |v8|, v35
	v_mfma_f32_32x32x16_bf16 v[32:47], v[64:67], v[124:127], 0
	v_fma_f32 v16, v157, |v17|, v16
	v_fma_f32 v24, v165, |v25|, v24
	v_fma_f32 v0, v173, |v1|, v0
	v_fma_f32 v8, v181, |v9|, v8
	v_fma_f32 v16, v155, |v18|, v16
	v_fma_f32 v24, v164, |v26|, v24
	v_fma_f32 v0, v172, |v2|, v0
	v_fma_f32 v8, v180, |v10|, v8
	s_waitcnt vmcnt(28)
; #define IDX_LOADG(BG, tb) do { _Pragma("unroll") for (int u = 0; u < 4; ++u) { int tt_ = (tb) + u; tt_ = tt_ < tile1 ? tt_ : tile1 - 1;        \
;               const bf16* kn = kp + (size_t)(tt_ - tile0) * 1024; BG[u][0] = *(const bf16x8*)kn; BG[u][1] = *(const bf16x8*)(kn + 16); } } while (0)
; #define IDX_TILES_NG(BG, tb) do { _Pragma("unroll") for (int u = 0; u < 4; ++u) IDX_ONE(BG, u, (tb) + u) } while (0)
; __device__ __forceinline__ void dsa2_unit(LAS unsigned char* lds, const bf16* PROJ, const bf16* KIDX, const bf16* KVN, bf16* OLAT, float* sbuf, int b, int t0, int tid) {
;     ...
;           if (tile0 < tile1) { bf16x8 BA[4][2], BB[4][2];
;               IDX_LOADG(BA, tile0);
;               int tileb = tile0;
;               for (; tileb + 8 <= tile1; tileb += 8) {
;                   IDX_LOADG(BB, tileb + 4);
;                   IDX_TILES_NG(BA, tileb);
;                   IDX_LOADG(BA, tileb + 8);
;                   IDX_TILES_NG(BB, tileb + 4); }
	v_mfma_f32_32x32x16_bf16 v[184:199], v[48:51], v[120:123], v[184:199]
	v_fma_f32 v16, v154, |v19|, v16
	v_fma_f32 v24, v163, |v27|, v24
	v_fma_f32 v0, v171, |v3|, v0
	v_fma_f32 v8, v179, |v11|, v8
	v_fma_f32 v16, v153, |v20|, v16
	v_fma_f32 v24, v162, |v28|, v24
	v_fma_f32 v0, v170, |v4|, v0
	v_fma_f32 v8, v178, |v12|, v8
	v_fma_f32 v16, v152, |v21|, v16
	v_mfma_f32_32x32x16_bf16 v[220:235], v[52:55], v[120:123], v[220:235]
	v_fma_f32 v24, v161, |v29|, v24
	v_fma_f32 v0, v169, |v5|, v0
	v_fma_f32 v8, v177, |v13|, v8
	v_fma_f32 v16, v151, |v22|, v16
	v_fma_f32 v24, v160, |v30|, v24
	v_fma_f32 v0, v168, |v6|, v0
	v_fma_f32 v8, v176, |v14|, v8
	v_fma_f32 v16, v139, |v23|, v16
	v_fma_f32 v24, v159, |v31|, v24
	v_mfma_f32_32x32x16_bf16 v[32:47], v[68:71], v[120:123], v[32:47]
	v_fma_f32 v0, v167, |v7|, v0
	v_fma_f32 v8, v175, |v15|, v8
	v_ashrrev_i32_e32 v210, 31, v16
	v_bitop3_b32 v16, v210, v16, s47 bitop3:0x36
	global_store_dword v[200:201], v16, off offset:512
	v_ashrrev_i32_e32 v211, 31, v24
	v_bitop3_b32 v24, v211, v24, s47 bitop3:0x36
	global_store_dword v[202:203], v24, off offset:512
	v_ashrrev_i32_e32 v210, 31, v0
	v_bitop3_b32 v0, v210, v0, s47 bitop3:0x36
	global_store_dword v[204:205], v0, off offset:512
	v_ashrrev_i32_e32 v211, 31, v8
	v_bitop3_b32 v8, v211, v8, s47 bitop3:0x36
	global_store_dword v[206:207], v8, off offset:512
	s_waitcnt vmcnt(31)
	v_mfma_f32_32x32x16_bf16 v[16:31], v[56:59], v[116:119], 0
	v_mfma_f32_32x32x16_bf16 v[0:15], v[60:63], v[116:119], 0
	s_nop 9
	v_fma_f32 v184, v158, |v184|, v32
	v_fma_f32 v192, v166, |v192|, v33
	v_fma_f32 v220, v174, |v220|, v34
	v_fma_f32 v228, v182, |v228|, v35
	v_mfma_f32_32x32x16_bf16 v[32:47], v[64:67], v[116:119], 0
	v_fma_f32 v184, v157, |v185|, v184
	v_fma_f32 v192, v165, |v193|, v192
	v_fma_f32 v220, v173, |v221|, v220
	v_fma_f32 v228, v181, |v229|, v228
	v_fma_f32 v184, v155, |v186|, v184
	v_fma_f32 v192, v164, |v194|, v192
	v_fma_f32 v220, v172, |v222|, v220
	v_fma_f32 v228, v180, |v230|, v228
	s_waitcnt vmcnt(30)
	v_mfma_f32_32x32x16_bf16 v[16:31], v[48:51], v[112:115], v[16:31]
	v_fma_f32 v184, v154, |v187|, v184
	v_fma_f32 v192, v163, |v195|, v192
	v_fma_f32 v220, v171, |v223|, v220
	v_fma_f32 v228, v179, |v231|, v228
	v_fma_f32 v184, v153, |v188|, v184
	v_fma_f32 v192, v162, |v196|, v192
	v_fma_f32 v220, v170, |v224|, v220
	v_fma_f32 v228, v178, |v232|, v228
	v_fma_f32 v184, v152, |v189|, v184
	v_mfma_f32_32x32x16_bf16 v[0:15], v[52:55], v[112:115], v[0:15]
	v_fma_f32 v192, v161, |v197|, v192
	v_fma_f32 v220, v169, |v225|, v220
	v_fma_f32 v228, v177, |v233|, v228
	v_fma_f32 v184, v151, |v190|, v184
	v_fma_f32 v192, v160, |v198|, v192
	v_fma_f32 v220, v168, |v226|, v220
	v_fma_f32 v228, v176, |v234|, v228
	v_fma_f32 v184, v139, |v191|, v184
	v_fma_f32 v192, v159, |v199|, v192
	v_mfma_f32_32x32x16_bf16 v[32:47], v[68:71], v[112:115], v[32:47]
	v_fma_f32 v220, v167, |v227|, v220
	v_fma_f32 v228, v175, |v235|, v228
	v_ashrrev_i32_e32 v210, 31, v184
	v_bitop3_b32 v184, v210, v184, s47 bitop3:0x36
	global_store_dword v[200:201], v184, off offset:640
	v_ashrrev_i32_e32 v211, 31, v192
	v_bitop3_b32 v192, v211, v192, s47 bitop3:0x36
	global_store_dword v[202:203], v192, off offset:640
	v_ashrrev_i32_e32 v210, 31, v220
	v_bitop3_b32 v220, v210, v220, s47 bitop3:0x36
	global_store_dword v[204:205], v220, off offset:640
	v_ashrrev_i32_e32 v211, 31, v228
	v_bitop3_b32 v228, v211, v228, s47 bitop3:0x36
	global_store_dword v[206:207], v228, off offset:640
	s_waitcnt vmcnt(33)
; #define IDX_LOADG(BG, tb) do { _Pragma("unroll") for (int u = 0; u < 4; ++u) { int tt_ = (tb) + u; tt_ = tt_ < tile1 ? tt_ : tile1 - 1;        \
;               const bf16* kn = kp + (size_t)(tt_ - tile0) * 1024; BG[u][0] = *(const bf16x8*)kn; BG[u][1] = *(const bf16x8*)(kn + 16); } } while (0)
; #define IDX_TILES_NG(BG, tb) do { _Pragma("unroll") for (int u = 0; u < 4; ++u) IDX_ONE(BG, u, (tb) + u) } while (0)
; __device__ __forceinline__ void dsa2_unit(LAS unsigned char* lds, const bf16* PROJ, const bf16* KIDX, const bf16* KVN, bf16* OLAT, float* sbuf, int b, int t0, int tid) {
;     ...
;           if (tile0 < tile1) { bf16x8 BA[4][2], BB[4][2];
;               IDX_LOADG(BA, tile0);
;               int tileb = tile0;
;               for (; tileb + 8 <= tile1; tileb += 8) {
;                   IDX_LOADG(BB, tileb + 4);
;                   IDX_TILES_NG(BA, tileb);
;                   IDX_LOADG(BA, tileb + 8);
;                   IDX_TILES_NG(BB, tileb + 4); }
	v_mfma_f32_32x32x16_bf16 v[184:199], v[56:59], v[108:111], 0
	v_mfma_f32_32x32x16_bf16 v[220:235], v[60:63], v[108:111], 0
	s_nop 9
	v_fma_f32 v16, v158, |v16|, v32
	v_fma_f32 v24, v166, |v24|, v33
	v_fma_f32 v0, v174, |v0|, v34
	v_fma_f32 v8, v182, |v8|, v35
	v_mfma_f32_32x32x16_bf16 v[32:47], v[64:67], v[108:111], 0
	v_fma_f32 v16, v157, |v17|, v16
	v_fma_f32 v24, v165, |v25|, v24
	v_fma_f32 v0, v173, |v1|, v0
	v_fma_f32 v8, v181, |v9|, v8
	v_fma_f32 v16, v155, |v18|, v16
	v_fma_f32 v24, v164, |v26|, v24
	v_fma_f32 v0, v172, |v2|, v0
	v_fma_f32 v8, v180, |v10|, v8
	s_waitcnt vmcnt(32)
	v_mfma_f32_32x32x16_bf16 v[184:199], v[48:51], v[104:107], v[184:199]
	v_fma_f32 v16, v154, |v19|, v16
	v_fma_f32 v24, v163, |v27|, v24
	v_fma_f32 v0, v171, |v3|, v0
	v_fma_f32 v8, v179, |v11|, v8
	v_fma_f32 v16, v153, |v20|, v16
	v_fma_f32 v24, v162, |v28|, v24
	v_fma_f32 v0, v170, |v4|, v0
	v_fma_f32 v8, v178, |v12|, v8
	v_fma_f32 v16, v152, |v21|, v16
	v_mfma_f32_32x32x16_bf16 v[220:235], v[52:55], v[104:107], v[220:235]
	v_fma_f32 v24, v161, |v29|, v24
	v_fma_f32 v0, v169, |v5|, v0
	v_fma_f32 v8, v177, |v13|, v8
	v_fma_f32 v16, v151, |v22|, v16
	v_fma_f32 v24, v160, |v30|, v24
	v_fma_f32 v0, v168, |v6|, v0
	v_fma_f32 v8, v176, |v14|, v8
	v_fma_f32 v16, v139, |v23|, v16
	v_fma_f32 v24, v159, |v31|, v24
	v_mfma_f32_32x32x16_bf16 v[32:47], v[68:71], v[104:107], v[32:47]
	v_fma_f32 v0, v167, |v7|, v0
	v_fma_f32 v8, v175, |v15|, v8
	v_ashrrev_i32_e32 v210, 31, v16
	v_bitop3_b32 v16, v210, v16, s47 bitop3:0x36
	global_store_dword v[200:201], v16, off offset:768
	v_ashrrev_i32_e32 v211, 31, v24
	v_bitop3_b32 v24, v211, v24, s47 bitop3:0x36
	global_store_dword v[202:203], v24, off offset:768
	v_ashrrev_i32_e32 v210, 31, v0
	v_bitop3_b32 v0, v210, v0, s47 bitop3:0x36
	global_store_dword v[204:205], v0, off offset:768
	v_ashrrev_i32_e32 v211, 31, v8
	v_bitop3_b32 v8, v211, v8, s47 bitop3:0x36
	global_store_dword v[206:207], v8, off offset:768
	s_nop 11
	v_fma_f32 v184, v158, |v184|, v32
	v_fma_f32 v192, v166, |v192|, v33
	v_fma_f32 v220, v174, |v220|, v34
	v_fma_f32 v228, v182, |v228|, v35
	v_fma_f32 v184, v157, |v185|, v184
	v_fma_f32 v192, v165, |v193|, v192
	v_fma_f32 v220, v173, |v221|, v220
	v_fma_f32 v228, v181, |v229|, v228
	v_fma_f32 v184, v155, |v186|, v184
	v_fma_f32 v192, v164, |v194|, v192
	v_fma_f32 v220, v172, |v222|, v220
	v_fma_f32 v228, v180, |v230|, v228
	v_fma_f32 v184, v154, |v187|, v184
	v_fma_f32 v192, v163, |v195|, v192
	v_fma_f32 v220, v171, |v223|, v220
	v_fma_f32 v228, v179, |v231|, v228
	v_fma_f32 v184, v153, |v188|, v184
	v_fma_f32 v192, v162, |v196|, v192
	v_fma_f32 v220, v170, |v224|, v220
	v_fma_f32 v228, v178, |v232|, v228
	v_fma_f32 v184, v152, |v189|, v184
	v_fma_f32 v192, v161, |v197|, v192
	v_fma_f32 v220, v169, |v225|, v220
	v_fma_f32 v228, v177, |v233|, v228
	v_fma_f32 v184, v151, |v190|, v184
	v_fma_f32 v192, v160, |v198|, v192
	v_fma_f32 v220, v168, |v226|, v220
	v_fma_f32 v228, v176, |v234|, v228
	v_fma_f32 v184, v139, |v191|, v184
	v_fma_f32 v192, v159, |v199|, v192
	v_fma_f32 v220, v167, |v227|, v220
	v_fma_f32 v228, v175, |v235|, v228
	v_ashrrev_i32_e32 v210, 31, v184
	v_bitop3_b32 v184, v210, v184, s47 bitop3:0x36
	global_store_dword v[200:201], v184, off offset:896
	v_ashrrev_i32_e32 v211, 31, v192
	v_bitop3_b32 v192, v211, v192, s47 bitop3:0x36
	global_store_dword v[202:203], v192, off offset:896
	v_ashrrev_i32_e32 v210, 31, v220
	v_bitop3_b32 v220, v210, v220, s47 bitop3:0x36
	global_store_dword v[204:205], v220, off offset:896
	v_ashrrev_i32_e32 v211, 31, v228
	v_bitop3_b32 v228, v211, v228, s47 bitop3:0x36
	global_store_dword v[206:207], v228, off offset:896
	s_add_i32 s4, s4, 8
	s_addk_i32 s6, 0x100
	s_add_i32 s5, s2, s4
	s_add_i32 s7, s5, 3
	s_cmp_le_i32 s7, s1
	s_cbranch_scc1 .LBB0_709
	s_add_i32 s8, s5, -5
	s_cmp_ge_i32 s8, s1
	s_cbranch_scc0 .LBB0_712
	s_branch .LBB0_720
